# expert-weight conversion: counted vmcnt keeps two 16 KB tiles in flight per wave instead of draining all three each loop trip
# speedup vs baseline: 1.0008x; 1.0008x over previous
; #define F8_LD(v, s_, d_, ok) do { ok = it < NEXP; if (ok) { f8_item(p, it, s_, d_); f8_tile_load(s_, v, lane); } it += stride; } while (0)
; __device__ __forceinline__ void convert_experts(const Params& p, int first, int stride, int lane) {
;     constexpr int NEXP = 3 * NE * 1024;
;     f32x4 va[16], vb[16], vc[16]; const float* sa; unsigned char* da; const float* sb; unsigned char* db; const float* sc; unsigned char* dc;
;     int it = first; bool oka, okb, okc;
;     ...
;     F8_LD(va, sa, da, oka); F8_LD(vb, sb, db, okb); F8_LD(vc, sc, dc, okc);
.LBB0_169:
	v_lshlrev_b32_e32 v1, 13, v0
	v_and_b32_e32 v194, 0xe000, v1
	v_lshlrev_b32_e32 v1, 1, v0
	s_add_u32 s21, s88, 0x1000000
	v_and_b32_e32 v198, 0x70, v1
	v_lshlrev_b32_e32 v1, 12, v0
	s_addc_u32 s22, s89, 0
	v_mov_b32_e32 v197, 0
	v_and_b32_e32 v200, 0x38000, v1
	v_lshlrev_b32_e32 v1, 2, v0
	s_add_u32 s23, s88, 0x2a800000
	s_mov_b32 s20, 0xe000
	v_mov_b32_e32 v195, v197
	v_mov_b32_e32 v199, v197
	v_and_b32_e32 v202, 28, v1
	s_addc_u32 s24, s89, 0
	s_mul_i32 s25, s27, 24
	s_lshl_b32 s26, s27, 5
	s_mul_i32 s27, s27, 40
	s_mov_b32 s28, 0xc3e00000
	v_mov_b32_e32 v1, 0x43e00000
	s_mov_b32 s29, 0x5010400
	s_mov_b32 s30, 0x7030602
	s_mov_b32 s31, 0x5040100
	s_mov_b32 s34, 0x7060302
	s_mov_b32 s35, 0x8000
	s_waitcnt vmcnt(0)
	s_branch .LBB0_173

; __device__ __forceinline__ float sat8(float x) { return __builtin_amdgcn_fmed3f(x, -448.0f, 448.0f); }
; __device__ __forceinline__ unsigned pk4_fp8(float a, float b, float c, float d) { int v = 0; v = __builtin_amdgcn_cvt_pk_fp8_f32(a, b, v, false); v = __builtin_amdgcn_cvt_pk_fp8_f32(c, d, v, true); return (unsigned)v; }
; __device__ __forceinline__ void f8_tile_store(const f32x4 (&v)[16], unsigned char* dst, int lane) {
;     unsigned d[16];
; #pragma unroll
;     for (int i = 0; i < 16; ++i) d[i] = pk4_fp8(sat8(v[i][0] * FP8_SW), sat8(v[i][1] * FP8_SW), sat8(v[i][2] * FP8_SW), sat8(v[i][3] * FP8_SW));
.LBB0_173:
	s_add_i32 s98, s27, s2
	s_cmp_lt_i32 s98, 0x18000
	s_cbranch_scc1 .Lconv_safe
	s_waitcnt vmcnt(0)
.Lconv_safe:
	s_waitcnt vmcnt(55)
	v_mul_f32_e32 v196, 0x43800000, v2
	v_mul_f32_e32 v201, 0x43800000, v3
	v_med3_f32 v196, v196, s28, v1
	v_med3_f32 v201, v201, s28, v1
	v_mov_b32_e32 v204, 0
	v_cvt_pk_fp8_f32 v204, v196, v201
	v_mul_f32_e32 v203, 0x43800000, v4
	v_mul_f32_e32 v201, 0x43800000, v5
	v_med3_f32 v196, v203, s28, v1
	v_med3_f32 v201, v201, s28, v1
	v_cvt_pk_fp8_f32 v204, v196, v201 op_sel:[0,0,1]
	s_waitcnt vmcnt(54)
	v_mul_f32_e32 v196, 0x43800000, v6
	v_mul_f32_e32 v201, 0x43800000, v7
	v_med3_f32 v196, v196, s28, v1
	v_med3_f32 v201, v201, s28, v1
	v_mov_b32_e32 v205, 0
	v_cvt_pk_fp8_f32 v205, v196, v201
	v_mul_f32_e32 v203, 0x43800000, v8
	v_mul_f32_e32 v201, 0x43800000, v9
	v_med3_f32 v196, v203, s28, v1
	v_med3_f32 v201, v201, s28, v1
	v_cvt_pk_fp8_f32 v205, v196, v201 op_sel:[0,0,1]
	s_waitcnt vmcnt(53)
	v_mul_f32_e32 v196, 0x43800000, v10
	v_mul_f32_e32 v201, 0x43800000, v11
	v_med3_f32 v196, v196, s28, v1
	v_med3_f32 v201, v201, s28, v1
	v_mov_b32_e32 v206, 0
	v_cvt_pk_fp8_f32 v206, v196, v201
	v_mul_f32_e32 v203, 0x43800000, v12
	v_mul_f32_e32 v201, 0x43800000, v13
	v_med3_f32 v196, v203, s28, v1
	v_med3_f32 v201, v201, s28, v1
	v_cvt_pk_fp8_f32 v206, v196, v201 op_sel:[0,0,1]
	s_waitcnt vmcnt(52)
	v_mul_f32_e32 v196, 0x43800000, v14
	v_mul_f32_e32 v201, 0x43800000, v15
	v_med3_f32 v196, v196, s28, v1
	v_med3_f32 v201, v201, s28, v1
	v_mov_b32_e32 v207, 0
	v_cvt_pk_fp8_f32 v207, v196, v201
	v_mul_f32_e32 v203, 0x43800000, v16
	v_mul_f32_e32 v201, 0x43800000, v17
	v_med3_f32 v196, v203, s28, v1
	v_med3_f32 v201, v201, s28, v1
	v_cvt_pk_fp8_f32 v207, v196, v201 op_sel:[0,0,1]
	s_waitcnt vmcnt(51)
	v_mul_f32_e32 v196, 0x43800000, v18
	v_mul_f32_e32 v201, 0x43800000, v19
	v_med3_f32 v196, v196, s28, v1
	v_med3_f32 v201, v201, s28, v1
	v_mov_b32_e32 v209, 0
	v_cvt_pk_fp8_f32 v209, v196, v201
	v_mul_f32_e32 v203, 0x43800000, v20
	v_mul_f32_e32 v201, 0x43800000, v21
	v_med3_f32 v196, v203, s28, v1
	v_med3_f32 v201, v201, s28, v1
	v_cvt_pk_fp8_f32 v209, v196, v201 op_sel:[0,0,1]
	s_waitcnt vmcnt(50)
	v_mul_f32_e32 v196, 0x43800000, v22
	v_mul_f32_e32 v201, 0x43800000, v23
	v_med3_f32 v196, v196, s28, v1
	v_med3_f32 v201, v201, s28, v1
	v_mov_b32_e32 v210, 0
	v_cvt_pk_fp8_f32 v210, v196, v201
	v_mul_f32_e32 v203, 0x43800000, v24
	v_mul_f32_e32 v201, 0x43800000, v25
	v_med3_f32 v196, v203, s28, v1
	v_med3_f32 v201, v201, s28, v1
	v_cvt_pk_fp8_f32 v210, v196, v201 op_sel:[0,0,1]
	s_waitcnt vmcnt(49)
	v_mul_f32_e32 v196, 0x43800000, v26
	v_mul_f32_e32 v201, 0x43800000, v27
	v_med3_f32 v196, v196, s28, v1
	v_med3_f32 v201, v201, s28, v1
	v_mov_b32_e32 v211, 0
	v_cvt_pk_fp8_f32 v211, v196, v201
	v_mul_f32_e32 v203, 0x43800000, v28
	v_mul_f32_e32 v201, 0x43800000, v29
	v_med3_f32 v196, v203, s28, v1
	v_med3_f32 v201, v201, s28, v1
	v_cvt_pk_fp8_f32 v211, v196, v201 op_sel:[0,0,1]
	s_waitcnt vmcnt(48)
	v_mul_f32_e32 v196, 0x43800000, v30
	v_mul_f32_e32 v201, 0x43800000, v31
	v_med3_f32 v196, v196, s28, v1
	v_med3_f32 v201, v201, s28, v1
	v_mov_b32_e32 v213, 0
	v_cvt_pk_fp8_f32 v213, v196, v201
	v_mul_f32_e32 v203, 0x43800000, v32
	v_mul_f32_e32 v201, 0x43800000, v33
	v_med3_f32 v196, v203, s28, v1
	v_med3_f32 v201, v201, s28, v1
	v_cvt_pk_fp8_f32 v213, v196, v201 op_sel:[0,0,1]
	s_waitcnt vmcnt(47)
	v_mul_f32_e32 v196, 0x43800000, v34
	v_mul_f32_e32 v201, 0x43800000, v35
	v_med3_f32 v196, v196, s28, v1
	v_med3_f32 v201, v201, s28, v1
	v_mov_b32_e32 v216, 0
	v_cvt_pk_fp8_f32 v216, v196, v201
	v_mul_f32_e32 v203, 0x43800000, v36
	v_mul_f32_e32 v201, 0x43800000, v37
	v_med3_f32 v196, v203, s28, v1
	v_med3_f32 v201, v201, s28, v1
	v_cvt_pk_fp8_f32 v216, v196, v201 op_sel:[0,0,1]
	s_waitcnt vmcnt(46)
	v_mul_f32_e32 v196, 0x43800000, v38
	v_mul_f32_e32 v201, 0x43800000, v39
	v_med3_f32 v196, v196, s28, v1
	v_med3_f32 v201, v201, s28, v1
	v_mov_b32_e32 v217, 0
	v_cvt_pk_fp8_f32 v217, v196, v201
	v_mul_f32_e32 v203, 0x43800000, v40
	v_mul_f32_e32 v201, 0x43800000, v41
	v_med3_f32 v196, v203, s28, v1
	v_med3_f32 v201, v201, s28, v1
	v_cvt_pk_fp8_f32 v217, v196, v201 op_sel:[0,0,1]
	s_waitcnt vmcnt(45)
	v_mul_f32_e32 v196, 0x43800000, v42
	v_mul_f32_e32 v201, 0x43800000, v43
	v_med3_f32 v196, v196, s28, v1
	v_med3_f32 v201, v201, s28, v1
	v_mov_b32_e32 v220, 0
	v_cvt_pk_fp8_f32 v220, v196, v201
	v_mul_f32_e32 v203, 0x43800000, v44
	v_mul_f32_e32 v201, 0x43800000, v45
	v_med3_f32 v196, v203, s28, v1
	v_med3_f32 v201, v201, s28, v1
	v_cvt_pk_fp8_f32 v220, v196, v201 op_sel:[0,0,1]
	s_waitcnt vmcnt(44)
	v_mul_f32_e32 v196, 0x43800000, v46
	v_mul_f32_e32 v201, 0x43800000, v47
	v_med3_f32 v196, v196, s28, v1
	v_med3_f32 v201, v201, s28, v1
	v_mov_b32_e32 v221, 0
	v_cvt_pk_fp8_f32 v221, v196, v201
	v_mul_f32_e32 v203, 0x43800000, v48
	v_mul_f32_e32 v201, 0x43800000, v49
	v_med3_f32 v196, v203, s28, v1
	v_med3_f32 v201, v201, s28, v1
	v_cvt_pk_fp8_f32 v221, v196, v201 op_sel:[0,0,1]
	s_waitcnt vmcnt(43)
; __device__ __forceinline__ float sat8(float x) { return __builtin_amdgcn_fmed3f(x, -448.0f, 448.0f); }
; __device__ __forceinline__ unsigned pk4_fp8(float a, float b, float c, float d) { int v = 0; v = __builtin_amdgcn_cvt_pk_fp8_f32(a, b, v, false); v = __builtin_amdgcn_cvt_pk_fp8_f32(c, d, v, true); return (unsigned)v; }
; __device__ __forceinline__ void f8_tile_store(const f32x4 (&v)[16], unsigned char* dst, int lane) {
;     unsigned d[16];
; #pragma unroll
;     for (int i = 0; i < 16; ++i) d[i] = pk4_fp8(sat8(v[i][0] * FP8_SW), sat8(v[i][1] * FP8_SW), sat8(v[i][2] * FP8_SW), sat8(v[i][3] * FP8_SW));
;     unsigned o[4][4];
; #pragma unroll
;     for (int w = 0; w < 4; ++w) {
;         const unsigned t0 = __builtin_amdgcn_perm(d[4 * w + 1], d[4 * w], 0x05010400u), t1 = __builtin_amdgcn_perm(d[4 * w + 1], d[4 * w], 0x07030602u);
;         const unsigned t2 = __builtin_amdgcn_perm(d[4 * w + 3], d[4 * w + 2], 0x05010400u), t3 = __builtin_amdgcn_perm(d[4 * w + 3], d[4 * w + 2], 0x07030602u);
;         o[0][w] = __builtin_amdgcn_perm(t2, t0, 0x05040100u); o[1][w] = __builtin_amdgcn_perm(t2, t0, 0x07060302u);
;         o[2][w] = __builtin_amdgcn_perm(t3, t1, 0x05040100u); o[3][w] = __builtin_amdgcn_perm(t3, t1, 0x07060302u);
;     }
;     unsigned char* d0 = dst + (size_t)(4 * (lane & 7)) * 2048 + 16 * (lane >> 3);
; #pragma unroll
;     for (int b = 0; b < 4; ++b) __builtin_nontemporal_store((v4u){o[b][0], o[b][1], o[b][2], o[b][3]}, (v4u*)(d0 + (size_t)b * 2048));
; }
; __device__ __forceinline__ void f8_item(const Params& p, int it, const float*& src, unsigned char*& dst) {
;     const int which = it >> 15, r = it & 32767, e = r >> 10, q = r & 1023, kb = q >> 6, nb = q & 63;
;     if (which == 2) { src = p.w_down + (size_t)e * FF * D + (size_t)(kb * 128) * D + nb * 32; dst = p.ws + WS_WD + ((size_t)e * D + nb * 32) * 2048 + kb * 128; }
;     else { const int f0 = nb * 32, drow = (f0 >> 7) * 256 + which * 128 + (f0 & 127);
;         src = (which == 0 ? p.w_gate : p.w_up) + (size_t)e * D * FF + (size_t)(kb * 128) * FF + f0; dst = p.ws + WS_WGU + ((size_t)e * 4096 + drow) * 2048 + kb * 128; }
; }
	v_mul_f32_e32 v196, 0x43800000, v50
	v_mul_f32_e32 v201, 0x43800000, v51
	v_med3_f32 v196, v196, s28, v1
	v_med3_f32 v201, v201, s28, v1
	v_mov_b32_e32 v222, 0
	v_cvt_pk_fp8_f32 v222, v196, v201
	v_mul_f32_e32 v203, 0x43800000, v52
	v_mul_f32_e32 v201, 0x43800000, v53
	v_med3_f32 v196, v203, s28, v1
	v_med3_f32 v201, v201, s28, v1
	v_cvt_pk_fp8_f32 v222, v196, v201 op_sel:[0,0,1]
	s_waitcnt vmcnt(42)
	v_mul_f32_e32 v196, 0x43800000, v54
	v_mul_f32_e32 v201, 0x43800000, v55
	v_med3_f32 v196, v196, s28, v1
	v_med3_f32 v201, v201, s28, v1
	v_mov_b32_e32 v223, 0
	v_cvt_pk_fp8_f32 v223, v196, v201
	v_mul_f32_e32 v203, 0x43800000, v56
	v_mul_f32_e32 v201, 0x43800000, v57
	v_med3_f32 v196, v203, s28, v1
	v_med3_f32 v201, v201, s28, v1
	v_cvt_pk_fp8_f32 v223, v196, v201 op_sel:[0,0,1]
	s_waitcnt vmcnt(41)
	v_mul_f32_e32 v196, 0x43800000, v58
	v_mul_f32_e32 v201, 0x43800000, v59
	v_med3_f32 v196, v196, s28, v1
	v_med3_f32 v201, v201, s28, v1
	v_mov_b32_e32 v224, 0
	v_cvt_pk_fp8_f32 v224, v196, v201
	v_mul_f32_e32 v203, 0x43800000, v60
	v_mul_f32_e32 v201, 0x43800000, v61
	v_med3_f32 v196, v203, s28, v1
	v_med3_f32 v201, v201, s28, v1
	v_cvt_pk_fp8_f32 v224, v196, v201 op_sel:[0,0,1]
	s_waitcnt vmcnt(40)
	v_mul_f32_e32 v196, 0x43800000, v62
	v_mul_f32_e32 v201, 0x43800000, v63
	v_med3_f32 v196, v196, s28, v1
	v_med3_f32 v201, v201, s28, v1
	v_mov_b32_e32 v225, 0
	v_cvt_pk_fp8_f32 v225, v196, v201
	v_mul_f32_e32 v203, 0x43800000, v64
	v_mul_f32_e32 v201, 0x43800000, v65
	v_med3_f32 v196, v203, s28, v1
	v_med3_f32 v201, v201, s28, v1
	v_cvt_pk_fp8_f32 v225, v196, v201 op_sel:[0,0,1]
	v_perm_b32 v196, v205, v204, s29
	v_perm_b32 v201, v205, v204, s30
	v_perm_b32 v203, v207, v206, s29
	v_perm_b32 v205, v207, v206, s30
	v_perm_b32 v204, v203, v196, s31
	v_perm_b32 v208, v203, v196, s34
	v_perm_b32 v214, v205, v201, s31
	v_perm_b32 v218, v205, v201, s34
	v_perm_b32 v196, v210, v209, s29
	v_perm_b32 v201, v210, v209, s30
	v_perm_b32 v203, v213, v211, s29
	v_perm_b32 v206, v213, v211, s30
	v_perm_b32 v205, v203, v196, s31
	v_perm_b32 v209, v203, v196, s34
	v_perm_b32 v215, v206, v201, s31
	v_perm_b32 v219, v206, v201, s34
	v_perm_b32 v196, v217, v216, s29
	v_perm_b32 v201, v217, v216, s30
	v_perm_b32 v203, v221, v220, s29
	v_perm_b32 v207, v221, v220, s30
	v_perm_b32 v206, v203, v196, s31
	v_perm_b32 v210, v203, v196, s34
	v_perm_b32 v216, v207, v201, s31
	v_perm_b32 v220, v207, v201, s34
	v_perm_b32 v196, v223, v222, s29
	v_perm_b32 v201, v223, v222, s30
	v_perm_b32 v203, v225, v224, s29
	v_lshl_add_u64 v[222:223], s[0:1], 0, v[194:195]
	s_add_i32 s36, s25, s2
	v_perm_b32 v207, v203, v196, s31
	v_lshl_add_u64 v[222:223], v[222:223], 0, v[198:199]
	v_perm_b32 v211, v203, v196, s34
	global_store_dwordx4 v[222:223], v[204:207], off nt
	global_store_dwordx4 v[222:223], v[208:211], off offset:2048 nt
	s_cmp_gt_i32 s36, 0x17fff
	v_add_co_u32_e32 v204, vcc, 0x1000, v222
	v_perm_b32 v213, v225, v224, s30
	s_nop 0
	v_addc_co_u32_e32 v205, vcc, 0, v223, vcc
	s_cselect_b64 s[14:15], -1, 0
	v_perm_b32 v217, v213, v201, s31
	s_and_b64 vcc, exec, s[14:15]
	v_perm_b32 v221, v213, v201, s34
	global_store_dwordx4 v[204:205], v[214:217], off nt
	global_store_dwordx4 v[204:205], v[218:221], off offset:2048 nt
	s_cbranch_vccnz .LBB0_179
	s_ashr_i32 s40, s36, 15
	s_bfe_u32 s37, s36, 0x5000a
	s_bfe_u32 s39, s36, 0x40006
	s_and_b32 s38, s36, 63
	s_cmp_lg_u32 s40, 2
	s_mov_b64 s[18:19], -1
	s_cbranch_scc0 .LBB0_176
	s_lshl_b32 s1, s38, 6
	s_lshl_b32 s0, s38, 5
	s_and_b32 s1, s1, 0xf00
	s_lshl_b32 s16, s40, 7
	s_add_i32 s1, s1, s16
	s_and_b32 s0, s0, 0x60
	s_or_b32 s0, s1, s0
	v_readlane_b32 s52, v255, 29
	s_cmpk_lt_u32 s36, 0x8000
	v_readlane_b32 s54, v255, 31
	v_readlane_b32 s55, v255, 32
	v_readlane_b32 s58, v255, 35
	v_readlane_b32 s59, v255, 36
	s_cselect_b32 s1, s55, s59
	s_cselect_b32 s16, s54, s58
	s_lshl_b32 s17, s37, 24
	s_add_u32 s16, s16, s17
	s_addc_u32 s1, s1, 0
	s_lshl_b32 s18, s39, 7
	s_lshl_b32 s17, s39, 20
	s_add_u32 s16, s16, s17
	s_addc_u32 s1, s1, 0
	s_lshl_b32 s17, s38, 7
	s_add_u32 s16, s16, s17
	s_addc_u32 s17, s1, 0
	s_ashr_i32 s1, s0, 31
	s_lshl_b32 s19, s37, 23
	s_lshl_b64 s[0:1], s[0:1], 11
	s_add_u32 s19, s21, s19
	s_addc_u32 s40, s22, 0
	s_add_u32 s0, s19, s0
	s_addc_u32 s1, s40, s1
	v_readlane_b32 s68, v255, 47
	s_add_u32 s0, s0, s18
	v_readlane_b32 s53, v255, 30
	v_readlane_b32 s56, v255, 33
	v_readlane_b32 s57, v255, 34
	v_readlane_b32 s60, v255, 37
	v_readlane_b32 s61, v255, 38
	v_readlane_b32 s62, v255, 39
	v_readlane_b32 s63, v255, 40
	v_readlane_b32 s64, v255, 41
	v_readlane_b32 s65, v255, 42
	v_readlane_b32 s66, v255, 43
	v_readlane_b32 s67, v255, 44
	v_readlane_b32 s69, v255, 48
	s_addc_u32 s1, s1, 0
	s_mov_b64 s[18:19], 0

; __device__ __forceinline__ float sat8(float x) { return __builtin_amdgcn_fmed3f(x, -448.0f, 448.0f); }
; __device__ __forceinline__ unsigned pk4_fp8(float a, float b, float c, float d) { int v = 0; v = __builtin_amdgcn_cvt_pk_fp8_f32(a, b, v, false); v = __builtin_amdgcn_cvt_pk_fp8_f32(c, d, v, true); return (unsigned)v; }
; #define F8_LD(v, s_, d_, ok) do { ok = it < NEXP; if (ok) { f8_item(p, it, s_, d_); f8_tile_load(s_, v, lane); } it += stride; } while (0)
; __device__ __forceinline__ void f8_tile_store(const f32x4 (&v)[16], unsigned char* dst, int lane) {
;     unsigned d[16];
; #pragma unroll
;     for (int i = 0; i < 16; ++i) d[i] = pk4_fp8(sat8(v[i][0] * FP8_SW), sat8(v[i][1] * FP8_SW), sat8(v[i][2] * FP8_SW), sat8(v[i][3] * FP8_SW));
; __device__ __forceinline__ void convert_experts(const Params& p, int first, int stride, int lane) {
;     ...
;         if (!oka) break; f8_tile_store(va, da, lane); F8_LD(va, sa, da, oka);
;         if (!okb) break; f8_tile_store(vb, db, lane); F8_LD(vb, sb, db, okb);
;         if (!okc) break; f8_tile_store(vc, dc, lane); F8_LD(vc, sc, dc, okc);
.LBB0_179:
	s_andn2_b64 vcc, exec, s[8:9]
	s_mov_b64 s[16:17], -1
	s_cbranch_vccnz .LBB0_172
	s_waitcnt vmcnt(40)
	v_mul_f32_e32 v196, 0x43800000, v66
	v_mul_f32_e32 v201, 0x43800000, v67
	v_med3_f32 v196, v196, s28, v1
	v_med3_f32 v201, v201, s28, v1
	v_mov_b32_e32 v204, v197
	v_cvt_pk_fp8_f32 v204, v196, v201
	v_mul_f32_e32 v203, 0x43800000, v68
	v_mul_f32_e32 v201, 0x43800000, v69
	v_med3_f32 v196, v203, s28, v1
	v_med3_f32 v201, v201, s28, v1
	v_cvt_pk_fp8_f32 v204, v196, v201 op_sel:[0,0,1]
	v_mul_f32_e32 v196, 0x43800000, v70
	v_mul_f32_e32 v201, 0x43800000, v71
	v_med3_f32 v196, v196, s28, v1
	v_med3_f32 v201, v201, s28, v1
	v_mov_b32_e32 v205, v197
	v_cvt_pk_fp8_f32 v205, v196, v201
	v_mul_f32_e32 v203, 0x43800000, v72
	v_mul_f32_e32 v201, 0x43800000, v73
	v_med3_f32 v196, v203, s28, v1
	v_med3_f32 v201, v201, s28, v1
	v_cvt_pk_fp8_f32 v205, v196, v201 op_sel:[0,0,1]
	v_mul_f32_e32 v196, 0x43800000, v74
	v_mul_f32_e32 v201, 0x43800000, v75
	v_med3_f32 v196, v196, s28, v1
	v_med3_f32 v201, v201, s28, v1
	v_mov_b32_e32 v206, v197
	v_cvt_pk_fp8_f32 v206, v196, v201
	v_mul_f32_e32 v203, 0x43800000, v76
	v_mul_f32_e32 v201, 0x43800000, v77
	v_med3_f32 v196, v203, s28, v1
	v_med3_f32 v201, v201, s28, v1
	v_cvt_pk_fp8_f32 v206, v196, v201 op_sel:[0,0,1]
	v_mul_f32_e32 v196, 0x43800000, v78
	v_mul_f32_e32 v201, 0x43800000, v79
	v_med3_f32 v196, v196, s28, v1
	v_med3_f32 v201, v201, s28, v1
	v_mov_b32_e32 v207, v197
	v_cvt_pk_fp8_f32 v207, v196, v201
	v_mul_f32_e32 v203, 0x43800000, v80
	v_mul_f32_e32 v201, 0x43800000, v81
	v_med3_f32 v196, v203, s28, v1
	v_med3_f32 v201, v201, s28, v1
	v_cvt_pk_fp8_f32 v207, v196, v201 op_sel:[0,0,1]
	v_mul_f32_e32 v196, 0x43800000, v82
	v_mul_f32_e32 v201, 0x43800000, v83
	v_med3_f32 v196, v196, s28, v1
	v_med3_f32 v201, v201, s28, v1
	v_mov_b32_e32 v209, v197
	v_cvt_pk_fp8_f32 v209, v196, v201
	v_mul_f32_e32 v203, 0x43800000, v84
	v_mul_f32_e32 v201, 0x43800000, v85
	v_med3_f32 v196, v203, s28, v1
	v_med3_f32 v201, v201, s28, v1
	v_cvt_pk_fp8_f32 v209, v196, v201 op_sel:[0,0,1]
	v_mul_f32_e32 v196, 0x43800000, v86
	v_mul_f32_e32 v201, 0x43800000, v87
	v_med3_f32 v196, v196, s28, v1
	v_med3_f32 v201, v201, s28, v1
	v_mov_b32_e32 v210, v197
	v_cvt_pk_fp8_f32 v210, v196, v201
	v_mul_f32_e32 v203, 0x43800000, v88
	v_mul_f32_e32 v201, 0x43800000, v89
	v_med3_f32 v196, v203, s28, v1
	v_med3_f32 v201, v201, s28, v1
	v_cvt_pk_fp8_f32 v210, v196, v201 op_sel:[0,0,1]
	v_mul_f32_e32 v196, 0x43800000, v90
	v_mul_f32_e32 v201, 0x43800000, v91
	v_med3_f32 v196, v196, s28, v1
	v_med3_f32 v201, v201, s28, v1
	v_mov_b32_e32 v211, v197
	v_cvt_pk_fp8_f32 v211, v196, v201
	v_mul_f32_e32 v203, 0x43800000, v92
	v_mul_f32_e32 v201, 0x43800000, v93
	v_med3_f32 v196, v203, s28, v1
	v_med3_f32 v201, v201, s28, v1
	v_cvt_pk_fp8_f32 v211, v196, v201 op_sel:[0,0,1]
	v_mul_f32_e32 v196, 0x43800000, v94
	v_mul_f32_e32 v201, 0x43800000, v95
	v_med3_f32 v196, v196, s28, v1
	v_med3_f32 v201, v201, s28, v1
	v_mov_b32_e32 v213, v197
	v_cvt_pk_fp8_f32 v213, v196, v201
	v_mul_f32_e32 v203, 0x43800000, v96
	v_mul_f32_e32 v201, 0x43800000, v97
	v_med3_f32 v196, v203, s28, v1
	v_med3_f32 v201, v201, s28, v1
	v_cvt_pk_fp8_f32 v213, v196, v201 op_sel:[0,0,1]
	v_mul_f32_e32 v196, 0x43800000, v98
	v_mul_f32_e32 v201, 0x43800000, v99
	v_med3_f32 v196, v196, s28, v1
	v_med3_f32 v201, v201, s28, v1
	v_mov_b32_e32 v216, v197
	v_cvt_pk_fp8_f32 v216, v196, v201
	v_mul_f32_e32 v203, 0x43800000, v100
	v_mul_f32_e32 v201, 0x43800000, v101
	v_med3_f32 v196, v203, s28, v1
	v_med3_f32 v201, v201, s28, v1
	v_cvt_pk_fp8_f32 v216, v196, v201 op_sel:[0,0,1]
	v_mul_f32_e32 v196, 0x43800000, v102
	v_mul_f32_e32 v201, 0x43800000, v103
	v_med3_f32 v196, v196, s28, v1
	v_med3_f32 v201, v201, s28, v1
	v_mov_b32_e32 v217, v197
	v_cvt_pk_fp8_f32 v217, v196, v201
	v_mul_f32_e32 v203, 0x43800000, v104
	v_mul_f32_e32 v201, 0x43800000, v105
	v_med3_f32 v196, v203, s28, v1
	v_med3_f32 v201, v201, s28, v1
	v_cvt_pk_fp8_f32 v217, v196, v201 op_sel:[0,0,1]
	v_mul_f32_e32 v196, 0x43800000, v106
	v_mul_f32_e32 v201, 0x43800000, v107
	v_med3_f32 v196, v196, s28, v1
	v_med3_f32 v201, v201, s28, v1
	v_mov_b32_e32 v220, v197
	v_cvt_pk_fp8_f32 v220, v196, v201
	v_mul_f32_e32 v203, 0x43800000, v108
	v_mul_f32_e32 v201, 0x43800000, v109
	v_med3_f32 v196, v203, s28, v1
	v_med3_f32 v201, v201, s28, v1
	v_cvt_pk_fp8_f32 v220, v196, v201 op_sel:[0,0,1]
	v_mul_f32_e32 v196, 0x43800000, v110
	v_mul_f32_e32 v201, 0x43800000, v111
	v_med3_f32 v196, v196, s28, v1
	v_med3_f32 v201, v201, s28, v1
	v_mov_b32_e32 v221, v197
	v_cvt_pk_fp8_f32 v221, v196, v201
	v_mul_f32_e32 v203, 0x43800000, v112
	v_mul_f32_e32 v201, 0x43800000, v113
	v_med3_f32 v196, v203, s28, v1
	v_med3_f32 v201, v201, s28, v1
; __device__ __forceinline__ float sat8(float x) { return __builtin_amdgcn_fmed3f(x, -448.0f, 448.0f); }
; __device__ __forceinline__ unsigned pk4_fp8(float a, float b, float c, float d) { int v = 0; v = __builtin_amdgcn_cvt_pk_fp8_f32(a, b, v, false); v = __builtin_amdgcn_cvt_pk_fp8_f32(c, d, v, true); return (unsigned)v; }
; __device__ __forceinline__ void f8_tile_store(const f32x4 (&v)[16], unsigned char* dst, int lane) {
;     ...
;     for (int i = 0; i < 16; ++i) d[i] = pk4_fp8(sat8(v[i][0] * FP8_SW), sat8(v[i][1] * FP8_SW), sat8(v[i][2] * FP8_SW), sat8(v[i][3] * FP8_SW));
;     unsigned o[4][4];
; #pragma unroll
;     for (int w = 0; w < 4; ++w) {
;         const unsigned t0 = __builtin_amdgcn_perm(d[4 * w + 1], d[4 * w], 0x05010400u), t1 = __builtin_amdgcn_perm(d[4 * w + 1], d[4 * w], 0x07030602u);
;         const unsigned t2 = __builtin_amdgcn_perm(d[4 * w + 3], d[4 * w + 2], 0x05010400u), t3 = __builtin_amdgcn_perm(d[4 * w + 3], d[4 * w + 2], 0x07030602u);
;         o[0][w] = __builtin_amdgcn_perm(t2, t0, 0x05040100u); o[1][w] = __builtin_amdgcn_perm(t2, t0, 0x07060302u);
;         o[2][w] = __builtin_amdgcn_perm(t3, t1, 0x05040100u); o[3][w] = __builtin_amdgcn_perm(t3, t1, 0x07060302u);
;     }
;     unsigned char* d0 = dst + (size_t)(4 * (lane & 7)) * 2048 + 16 * (lane >> 3);
; #pragma unroll
;     for (int b = 0; b < 4; ++b) __builtin_nontemporal_store((v4u){o[b][0], o[b][1], o[b][2], o[b][3]}, (v4u*)(d0 + (size_t)b * 2048));
; }
; __device__ __forceinline__ void f8_item(const Params& p, int it, const float*& src, unsigned char*& dst) {
;     const int which = it >> 15, r = it & 32767, e = r >> 10, q = r & 1023, kb = q >> 6, nb = q & 63;
;     if (which == 2) { src = p.w_down + (size_t)e * FF * D + (size_t)(kb * 128) * D + nb * 32; dst = p.ws + WS_WD + ((size_t)e * D + nb * 32) * 2048 + kb * 128; }
;     else { const int f0 = nb * 32, drow = (f0 >> 7) * 256 + which * 128 + (f0 & 127);
;         src = (which == 0 ? p.w_gate : p.w_up) + (size_t)e * D * FF + (size_t)(kb * 128) * FF + f0; dst = p.ws + WS_WGU + ((size_t)e * 4096 + drow) * 2048 + kb * 128; }
; }
	v_cvt_pk_fp8_f32 v221, v196, v201 op_sel:[0,0,1]
	v_mul_f32_e32 v196, 0x43800000, v114
	v_mul_f32_e32 v201, 0x43800000, v115
	v_med3_f32 v196, v196, s28, v1
	v_med3_f32 v201, v201, s28, v1
	v_mov_b32_e32 v222, v197
	v_cvt_pk_fp8_f32 v222, v196, v201
	v_mul_f32_e32 v203, 0x43800000, v116
	v_mul_f32_e32 v201, 0x43800000, v117
	v_med3_f32 v196, v203, s28, v1
	v_med3_f32 v201, v201, s28, v1
	v_cvt_pk_fp8_f32 v222, v196, v201 op_sel:[0,0,1]
	v_mul_f32_e32 v196, 0x43800000, v118
	v_mul_f32_e32 v201, 0x43800000, v119
	v_med3_f32 v196, v196, s28, v1
	v_med3_f32 v201, v201, s28, v1
	v_mov_b32_e32 v223, v197
	v_cvt_pk_fp8_f32 v223, v196, v201
	v_mul_f32_e32 v203, 0x43800000, v120
	v_mul_f32_e32 v201, 0x43800000, v121
	v_med3_f32 v196, v203, s28, v1
	v_med3_f32 v201, v201, s28, v1
	v_cvt_pk_fp8_f32 v223, v196, v201 op_sel:[0,0,1]
	v_mul_f32_e32 v196, 0x43800000, v122
	v_mul_f32_e32 v201, 0x43800000, v123
	v_med3_f32 v196, v196, s28, v1
	v_med3_f32 v201, v201, s28, v1
	v_mov_b32_e32 v224, v197
	v_cvt_pk_fp8_f32 v224, v196, v201
	v_mul_f32_e32 v203, 0x43800000, v124
	v_mul_f32_e32 v201, 0x43800000, v125
	v_med3_f32 v196, v203, s28, v1
	v_med3_f32 v201, v201, s28, v1
	v_cvt_pk_fp8_f32 v224, v196, v201 op_sel:[0,0,1]
	v_mul_f32_e32 v196, 0x43800000, v126
	v_mul_f32_e32 v201, 0x43800000, v127
	v_med3_f32 v196, v196, s28, v1
	v_med3_f32 v201, v201, s28, v1
	v_mov_b32_e32 v225, v197
	v_cvt_pk_fp8_f32 v225, v196, v201
	v_mul_f32_e32 v203, 0x43800000, v128
	v_mul_f32_e32 v201, 0x43800000, v129
	v_med3_f32 v196, v203, s28, v1
	v_med3_f32 v201, v201, s28, v1
	v_cvt_pk_fp8_f32 v225, v196, v201 op_sel:[0,0,1]
	v_perm_b32 v196, v205, v204, s29
	v_perm_b32 v201, v205, v204, s30
	v_perm_b32 v203, v207, v206, s29
	v_perm_b32 v205, v207, v206, s30
	v_perm_b32 v204, v203, v196, s31
	v_perm_b32 v208, v203, v196, s34
	v_perm_b32 v214, v205, v201, s31
	v_perm_b32 v218, v205, v201, s34
	v_perm_b32 v196, v210, v209, s29
	v_perm_b32 v201, v210, v209, s30
	v_perm_b32 v203, v213, v211, s29
	v_perm_b32 v206, v213, v211, s30
	v_perm_b32 v205, v203, v196, s31
	v_perm_b32 v209, v203, v196, s34
	v_perm_b32 v215, v206, v201, s31
	v_perm_b32 v219, v206, v201, s34
	v_perm_b32 v196, v217, v216, s29
	v_perm_b32 v201, v217, v216, s30
	v_perm_b32 v203, v221, v220, s29
	v_perm_b32 v207, v221, v220, s30
	v_perm_b32 v206, v203, v196, s31
	v_perm_b32 v210, v203, v196, s34
	v_perm_b32 v216, v207, v201, s31
	v_perm_b32 v220, v207, v201, s34
	v_perm_b32 v196, v223, v222, s29
	v_perm_b32 v201, v223, v222, s30
	v_perm_b32 v203, v225, v224, s29
	v_lshl_add_u64 v[222:223], s[6:7], 0, v[194:195]
	s_add_i32 s37, s26, s2
	v_perm_b32 v207, v203, v196, s31
	v_lshl_add_u64 v[222:223], v[222:223], 0, v[198:199]
	v_perm_b32 v213, v225, v224, s30
	v_perm_b32 v211, v203, v196, s34
	global_store_dwordx4 v[222:223], v[204:207], off nt
	global_store_dwordx4 v[222:223], v[208:211], off offset:2048 nt
	s_cmp_lt_i32 s37, 0x18000
	v_add_co_u32_e32 v204, vcc, 0x1000, v222
	v_perm_b32 v217, v213, v201, s31
	v_perm_b32 v221, v213, v201, s34
	v_addc_co_u32_e32 v205, vcc, 0, v223, vcc
	s_cselect_b64 s[8:9], -1, 0
	s_cmp_gt_i32 s37, 0x17fff
	global_store_dwordx4 v[204:205], v[214:217], off nt
	global_store_dwordx4 v[204:205], v[218:221], off offset:2048 nt
	s_cbranch_scc1 .LBB0_186
	s_ashr_i32 s41, s37, 15
	s_bfe_u32 s38, s37, 0x5000a
	s_bfe_u32 s40, s37, 0x40006
	s_and_b32 s39, s37, 63
	s_cmp_lg_u32 s41, 2
	s_mov_b64 s[18:19], -1
	s_cbranch_scc0 .LBB0_183
	s_lshl_b32 s7, s39, 6
	s_lshl_b32 s6, s39, 5
	s_and_b32 s7, s7, 0xf00
	s_lshl_b32 s16, s41, 7
	s_add_i32 s7, s7, s16
	s_and_b32 s6, s6, 0x60
	s_or_b32 s6, s7, s6
	v_readlane_b32 s52, v255, 29
	s_cmpk_lt_u32 s37, 0x8000
	v_readlane_b32 s54, v255, 31
	v_readlane_b32 s55, v255, 32
	v_readlane_b32 s58, v255, 35
	v_readlane_b32 s59, v255, 36
	s_cselect_b32 s7, s55, s59
	s_cselect_b32 s16, s54, s58
	s_lshl_b32 s17, s38, 24
	s_add_u32 s16, s16, s17
	s_addc_u32 s7, s7, 0
	s_lshl_b32 s18, s40, 7
	s_lshl_b32 s17, s40, 20
	s_add_u32 s16, s16, s17
	s_addc_u32 s7, s7, 0
	s_lshl_b32 s17, s39, 7
	s_add_u32 s16, s16, s17
	s_addc_u32 s17, s7, 0
	s_ashr_i32 s7, s6, 31
	s_lshl_b32 s19, s38, 23
	s_lshl_b64 s[6:7], s[6:7], 11
	s_add_u32 s19, s21, s19
	s_addc_u32 s37, s22, 0
	s_add_u32 s6, s19, s6
	s_addc_u32 s7, s37, s7
	v_readlane_b32 s68, v255, 47
	s_add_u32 s6, s6, s18
	v_readlane_b32 s53, v255, 30
	v_readlane_b32 s56, v255, 33
	v_readlane_b32 s57, v255, 34
	v_readlane_b32 s60, v255, 37
	v_readlane_b32 s61, v255, 38
	v_readlane_b32 s62, v255, 39
	v_readlane_b32 s63, v255, 40
	v_readlane_b32 s64, v255, 41
	v_readlane_b32 s65, v255, 42
	v_readlane_b32 s66, v255, 43
	v_readlane_b32 s67, v255, 44
	v_readlane_b32 s69, v255, 48
	s_addc_u32 s7, s7, 0
	s_mov_b64 s[18:19], 0

; __device__ __forceinline__ float sat8(float x) { return __builtin_amdgcn_fmed3f(x, -448.0f, 448.0f); }
; __device__ __forceinline__ unsigned pk4_fp8(float a, float b, float c, float d) { int v = 0; v = __builtin_amdgcn_cvt_pk_fp8_f32(a, b, v, false); v = __builtin_amdgcn_cvt_pk_fp8_f32(c, d, v, true); return (unsigned)v; }
; #define F8_LD(v, s_, d_, ok) do { ok = it < NEXP; if (ok) { f8_item(p, it, s_, d_); f8_tile_load(s_, v, lane); } it += stride; } while (0)
; __device__ __forceinline__ void f8_tile_store(const f32x4 (&v)[16], unsigned char* dst, int lane) {
;     unsigned d[16];
; #pragma unroll
;     for (int i = 0; i < 16; ++i) d[i] = pk4_fp8(sat8(v[i][0] * FP8_SW), sat8(v[i][1] * FP8_SW), sat8(v[i][2] * FP8_SW), sat8(v[i][3] * FP8_SW));
; __device__ __forceinline__ void convert_experts(const Params& p, int first, int stride, int lane) {
;     ...
;         if (!oka) break; f8_tile_store(va, da, lane); F8_LD(va, sa, da, oka);
;         if (!okb) break; f8_tile_store(vb, db, lane); F8_LD(vb, sb, db, okb);
;         if (!okc) break; f8_tile_store(vc, dc, lane); F8_LD(vc, sc, dc, okc);
.LBB0_186:
	s_andn2_b64 vcc, exec, s[12:13]
	s_mov_b64 s[16:17], -1
	s_cbranch_vccnz .LBB0_172
	s_waitcnt vmcnt(40)
	v_mul_f32_e32 v196, 0x43800000, v130
	v_mul_f32_e32 v201, 0x43800000, v131
	v_med3_f32 v196, v196, s28, v1
	v_med3_f32 v201, v201, s28, v1
	v_mov_b32_e32 v204, v197
	v_cvt_pk_fp8_f32 v204, v196, v201
	v_mul_f32_e32 v203, 0x43800000, v132
	v_mul_f32_e32 v201, 0x43800000, v133
	v_med3_f32 v196, v203, s28, v1
	v_med3_f32 v201, v201, s28, v1
	v_cvt_pk_fp8_f32 v204, v196, v201 op_sel:[0,0,1]
	v_mul_f32_e32 v196, 0x43800000, v134
	v_mul_f32_e32 v201, 0x43800000, v135
	v_med3_f32 v196, v196, s28, v1
	v_med3_f32 v201, v201, s28, v1
	v_mov_b32_e32 v205, v197
	v_cvt_pk_fp8_f32 v205, v196, v201
	v_mul_f32_e32 v203, 0x43800000, v136
	v_mul_f32_e32 v201, 0x43800000, v137
	v_med3_f32 v196, v203, s28, v1
	v_med3_f32 v201, v201, s28, v1
	v_cvt_pk_fp8_f32 v205, v196, v201 op_sel:[0,0,1]
	v_mul_f32_e32 v196, 0x43800000, v138
	v_mul_f32_e32 v201, 0x43800000, v139
	v_med3_f32 v196, v196, s28, v1
	v_med3_f32 v201, v201, s28, v1
	v_mov_b32_e32 v206, v197
	v_cvt_pk_fp8_f32 v206, v196, v201
	v_mul_f32_e32 v203, 0x43800000, v140
	v_mul_f32_e32 v201, 0x43800000, v141
	v_med3_f32 v196, v203, s28, v1
	v_med3_f32 v201, v201, s28, v1
	v_cvt_pk_fp8_f32 v206, v196, v201 op_sel:[0,0,1]
	v_mul_f32_e32 v196, 0x43800000, v142
	v_mul_f32_e32 v201, 0x43800000, v143
	v_med3_f32 v196, v196, s28, v1
	v_med3_f32 v201, v201, s28, v1
	v_mov_b32_e32 v207, v197
	v_cvt_pk_fp8_f32 v207, v196, v201
	v_mul_f32_e32 v203, 0x43800000, v144
	v_mul_f32_e32 v201, 0x43800000, v145
	v_med3_f32 v196, v203, s28, v1
	v_med3_f32 v201, v201, s28, v1
	v_cvt_pk_fp8_f32 v207, v196, v201 op_sel:[0,0,1]
	v_mul_f32_e32 v196, 0x43800000, v146
	v_mul_f32_e32 v201, 0x43800000, v147
	v_med3_f32 v196, v196, s28, v1
	v_med3_f32 v201, v201, s28, v1
	v_mov_b32_e32 v209, v197
	v_cvt_pk_fp8_f32 v209, v196, v201
	v_mul_f32_e32 v203, 0x43800000, v148
	v_mul_f32_e32 v201, 0x43800000, v149
	v_med3_f32 v196, v203, s28, v1
	v_med3_f32 v201, v201, s28, v1
	v_cvt_pk_fp8_f32 v209, v196, v201 op_sel:[0,0,1]
	v_mul_f32_e32 v196, 0x43800000, v150
	v_mul_f32_e32 v201, 0x43800000, v151
	v_med3_f32 v196, v196, s28, v1
	v_med3_f32 v201, v201, s28, v1
	v_mov_b32_e32 v210, v197
	v_cvt_pk_fp8_f32 v210, v196, v201
	v_mul_f32_e32 v203, 0x43800000, v152
	v_mul_f32_e32 v201, 0x43800000, v153
	v_med3_f32 v196, v203, s28, v1
	v_med3_f32 v201, v201, s28, v1
	v_cvt_pk_fp8_f32 v210, v196, v201 op_sel:[0,0,1]
	v_mul_f32_e32 v196, 0x43800000, v154
	v_mul_f32_e32 v201, 0x43800000, v155
	v_med3_f32 v196, v196, s28, v1
	v_med3_f32 v201, v201, s28, v1
	v_mov_b32_e32 v211, v197
	v_cvt_pk_fp8_f32 v211, v196, v201
	v_mul_f32_e32 v203, 0x43800000, v156
	v_mul_f32_e32 v201, 0x43800000, v157
	v_med3_f32 v196, v203, s28, v1
	v_med3_f32 v201, v201, s28, v1
	v_cvt_pk_fp8_f32 v211, v196, v201 op_sel:[0,0,1]
	v_mul_f32_e32 v196, 0x43800000, v158
	v_mul_f32_e32 v201, 0x43800000, v159
	v_med3_f32 v196, v196, s28, v1
	v_med3_f32 v201, v201, s28, v1
	v_mov_b32_e32 v213, v197
	v_cvt_pk_fp8_f32 v213, v196, v201
	v_mul_f32_e32 v203, 0x43800000, v160
	v_mul_f32_e32 v201, 0x43800000, v161
	v_med3_f32 v196, v203, s28, v1
	v_med3_f32 v201, v201, s28, v1
	v_cvt_pk_fp8_f32 v213, v196, v201 op_sel:[0,0,1]
	v_mul_f32_e32 v196, 0x43800000, v162
	v_mul_f32_e32 v201, 0x43800000, v163
	v_med3_f32 v196, v196, s28, v1
	v_med3_f32 v201, v201, s28, v1
	v_mov_b32_e32 v216, v197
	v_cvt_pk_fp8_f32 v216, v196, v201
	v_mul_f32_e32 v203, 0x43800000, v164
	v_mul_f32_e32 v201, 0x43800000, v165
	v_med3_f32 v196, v203, s28, v1
	v_med3_f32 v201, v201, s28, v1
	v_cvt_pk_fp8_f32 v216, v196, v201 op_sel:[0,0,1]
	v_mul_f32_e32 v196, 0x43800000, v166
	v_mul_f32_e32 v201, 0x43800000, v167
	v_med3_f32 v196, v196, s28, v1
	v_med3_f32 v201, v201, s28, v1
	v_mov_b32_e32 v217, v197
	v_cvt_pk_fp8_f32 v217, v196, v201
	v_mul_f32_e32 v203, 0x43800000, v168
	v_mul_f32_e32 v201, 0x43800000, v169
	v_med3_f32 v196, v203, s28, v1
	v_med3_f32 v201, v201, s28, v1
	v_cvt_pk_fp8_f32 v217, v196, v201 op_sel:[0,0,1]
	v_mul_f32_e32 v196, 0x43800000, v170
	v_mul_f32_e32 v201, 0x43800000, v171
	v_med3_f32 v196, v196, s28, v1
	v_med3_f32 v201, v201, s28, v1
	v_mov_b32_e32 v220, v197
	v_cvt_pk_fp8_f32 v220, v196, v201
	v_mul_f32_e32 v203, 0x43800000, v172
	v_mul_f32_e32 v201, 0x43800000, v173
	v_med3_f32 v196, v203, s28, v1
	v_med3_f32 v201, v201, s28, v1
	v_cvt_pk_fp8_f32 v220, v196, v201 op_sel:[0,0,1]
	v_mul_f32_e32 v196, 0x43800000, v174
	v_mul_f32_e32 v201, 0x43800000, v175
	v_med3_f32 v196, v196, s28, v1
	v_med3_f32 v201, v201, s28, v1
	v_mov_b32_e32 v221, v197
	v_cvt_pk_fp8_f32 v221, v196, v201
	v_mul_f32_e32 v203, 0x43800000, v176
	v_mul_f32_e32 v201, 0x43800000, v177
	v_med3_f32 v196, v203, s28, v1
; __device__ __forceinline__ float sat8(float x) { return __builtin_amdgcn_fmed3f(x, -448.0f, 448.0f); }
; __device__ __forceinline__ unsigned pk4_fp8(float a, float b, float c, float d) { int v = 0; v = __builtin_amdgcn_cvt_pk_fp8_f32(a, b, v, false); v = __builtin_amdgcn_cvt_pk_fp8_f32(c, d, v, true); return (unsigned)v; }
; __device__ __forceinline__ void f8_tile_store(const f32x4 (&v)[16], unsigned char* dst, int lane) {
;     ...
;     for (int i = 0; i < 16; ++i) d[i] = pk4_fp8(sat8(v[i][0] * FP8_SW), sat8(v[i][1] * FP8_SW), sat8(v[i][2] * FP8_SW), sat8(v[i][3] * FP8_SW));
;     unsigned o[4][4];
; #pragma unroll
;     for (int w = 0; w < 4; ++w) {
;         const unsigned t0 = __builtin_amdgcn_perm(d[4 * w + 1], d[4 * w], 0x05010400u), t1 = __builtin_amdgcn_perm(d[4 * w + 1], d[4 * w], 0x07030602u);
;         const unsigned t2 = __builtin_amdgcn_perm(d[4 * w + 3], d[4 * w + 2], 0x05010400u), t3 = __builtin_amdgcn_perm(d[4 * w + 3], d[4 * w + 2], 0x07030602u);
;         o[0][w] = __builtin_amdgcn_perm(t2, t0, 0x05040100u); o[1][w] = __builtin_amdgcn_perm(t2, t0, 0x07060302u);
;         o[2][w] = __builtin_amdgcn_perm(t3, t1, 0x05040100u); o[3][w] = __builtin_amdgcn_perm(t3, t1, 0x07060302u);
;     }
;     unsigned char* d0 = dst + (size_t)(4 * (lane & 7)) * 2048 + 16 * (lane >> 3);
; #pragma unroll
;     for (int b = 0; b < 4; ++b) __builtin_nontemporal_store((v4u){o[b][0], o[b][1], o[b][2], o[b][3]}, (v4u*)(d0 + (size_t)b * 2048));
; }
; __device__ __forceinline__ void f8_item(const Params& p, int it, const float*& src, unsigned char*& dst) {
;     const int which = it >> 15, r = it & 32767, e = r >> 10, q = r & 1023, kb = q >> 6, nb = q & 63;
;     if (which == 2) { src = p.w_down + (size_t)e * FF * D + (size_t)(kb * 128) * D + nb * 32; dst = p.ws + WS_WD + ((size_t)e * D + nb * 32) * 2048 + kb * 128; }
;     else { const int f0 = nb * 32, drow = (f0 >> 7) * 256 + which * 128 + (f0 & 127);
;         src = (which == 0 ? p.w_gate : p.w_up) + (size_t)e * D * FF + (size_t)(kb * 128) * FF + f0; dst = p.ws + WS_WGU + ((size_t)e * 4096 + drow) * 2048 + kb * 128; }
; }
	v_med3_f32 v201, v201, s28, v1
	v_cvt_pk_fp8_f32 v221, v196, v201 op_sel:[0,0,1]
	v_mul_f32_e32 v196, 0x43800000, v178
	v_mul_f32_e32 v201, 0x43800000, v179
	v_med3_f32 v196, v196, s28, v1
	v_med3_f32 v201, v201, s28, v1
	v_mov_b32_e32 v222, v197
	v_cvt_pk_fp8_f32 v222, v196, v201
	v_mul_f32_e32 v203, 0x43800000, v180
	v_mul_f32_e32 v201, 0x43800000, v181
	v_med3_f32 v196, v203, s28, v1
	v_med3_f32 v201, v201, s28, v1
	v_cvt_pk_fp8_f32 v222, v196, v201 op_sel:[0,0,1]
	v_mul_f32_e32 v196, 0x43800000, v182
	v_mul_f32_e32 v201, 0x43800000, v183
	v_med3_f32 v196, v196, s28, v1
	v_med3_f32 v201, v201, s28, v1
	v_mov_b32_e32 v223, v197
	v_cvt_pk_fp8_f32 v223, v196, v201
	v_mul_f32_e32 v203, 0x43800000, v184
	v_mul_f32_e32 v201, 0x43800000, v185
	v_med3_f32 v196, v203, s28, v1
	v_med3_f32 v201, v201, s28, v1
	v_cvt_pk_fp8_f32 v223, v196, v201 op_sel:[0,0,1]
	v_mul_f32_e32 v196, 0x43800000, v186
	v_mul_f32_e32 v201, 0x43800000, v187
	v_med3_f32 v196, v196, s28, v1
	v_med3_f32 v201, v201, s28, v1
	v_mov_b32_e32 v224, v197
	v_cvt_pk_fp8_f32 v224, v196, v201
	v_mul_f32_e32 v203, 0x43800000, v188
	v_mul_f32_e32 v201, 0x43800000, v189
	v_med3_f32 v196, v203, s28, v1
	v_med3_f32 v201, v201, s28, v1
	v_cvt_pk_fp8_f32 v224, v196, v201 op_sel:[0,0,1]
	v_mul_f32_e32 v196, 0x43800000, v190
	v_mul_f32_e32 v201, 0x43800000, v191
	v_med3_f32 v196, v196, s28, v1
	v_med3_f32 v201, v201, s28, v1
	v_mov_b32_e32 v225, v197
	v_cvt_pk_fp8_f32 v225, v196, v201
	v_mul_f32_e32 v203, 0x43800000, v192
	v_mul_f32_e32 v201, 0x43800000, v193
	v_med3_f32 v196, v203, s28, v1
	v_med3_f32 v201, v201, s28, v1
	v_cvt_pk_fp8_f32 v225, v196, v201 op_sel:[0,0,1]
	v_perm_b32 v196, v205, v204, s29
	v_perm_b32 v201, v205, v204, s30
	v_perm_b32 v203, v207, v206, s29
	v_perm_b32 v205, v207, v206, s30
	v_perm_b32 v204, v203, v196, s31
	v_perm_b32 v208, v203, v196, s34
	v_perm_b32 v214, v205, v201, s31
	v_perm_b32 v218, v205, v201, s34
	v_perm_b32 v196, v210, v209, s29
	v_perm_b32 v201, v210, v209, s30
	v_perm_b32 v203, v213, v211, s29
	v_perm_b32 v206, v213, v211, s30
	v_perm_b32 v205, v203, v196, s31
	v_perm_b32 v209, v203, v196, s34
	v_perm_b32 v215, v206, v201, s31
	v_perm_b32 v219, v206, v201, s34
	v_perm_b32 v196, v217, v216, s29
	v_perm_b32 v201, v217, v216, s30
	v_perm_b32 v203, v221, v220, s29
	v_perm_b32 v207, v221, v220, s30
	v_perm_b32 v206, v203, v196, s31
	v_perm_b32 v210, v203, v196, s34
	v_perm_b32 v216, v207, v201, s31
	v_perm_b32 v220, v207, v201, s34
	v_perm_b32 v196, v223, v222, s29
	v_perm_b32 v201, v223, v222, s30
	v_perm_b32 v203, v225, v224, s29
	v_lshl_add_u64 v[222:223], s[10:11], 0, v[194:195]
	s_add_i32 s2, s27, s2
	v_perm_b32 v207, v203, v196, s31
	v_lshl_add_u64 v[222:223], v[222:223], 0, v[198:199]
	v_perm_b32 v213, v225, v224, s30
	v_perm_b32 v211, v203, v196, s34
	global_store_dwordx4 v[222:223], v[204:207], off nt
	global_store_dwordx4 v[222:223], v[208:211], off offset:2048 nt
	s_cmp_lt_i32 s2, 0x18000
	v_add_co_u32_e32 v204, vcc, 0x1000, v222
	v_perm_b32 v217, v213, v201, s31
	v_perm_b32 v221, v213, v201, s34
	v_addc_co_u32_e32 v205, vcc, 0, v223, vcc
	s_cselect_b64 s[12:13], -1, 0
	s_cmp_gt_i32 s2, 0x17fff
	global_store_dwordx4 v[204:205], v[214:217], off nt
	global_store_dwordx4 v[204:205], v[218:221], off offset:2048 nt
	s_cbranch_scc1 .LBB0_171
	s_ashr_i32 s40, s2, 15
	s_bfe_u32 s37, s2, 0x5000a
	s_bfe_u32 s39, s2, 0x40006
	s_and_b32 s38, s2, 63
	s_cmp_lg_u32 s40, 2
	s_mov_b64 s[18:19], -1
	s_cbranch_scc0 .LBB0_190
	s_lshl_b32 s11, s38, 6
	s_lshl_b32 s10, s38, 5
	s_and_b32 s11, s11, 0xf00
	s_lshl_b32 s16, s40, 7
	s_add_i32 s11, s11, s16
	s_and_b32 s10, s10, 0x60
	s_or_b32 s10, s11, s10
	v_readlane_b32 s52, v255, 29
	s_cmpk_lt_u32 s2, 0x8000
	v_readlane_b32 s54, v255, 31
	v_readlane_b32 s55, v255, 32
	v_readlane_b32 s58, v255, 35
	v_readlane_b32 s59, v255, 36
	s_cselect_b32 s2, s55, s59
	s_cselect_b32 s11, s54, s58
	s_lshl_b32 s16, s37, 24
	s_add_u32 s11, s11, s16
	s_addc_u32 s2, s2, 0
	s_lshl_b32 s18, s39, 7
	s_lshl_b32 s16, s39, 20
	s_add_u32 s11, s11, s16
	s_addc_u32 s2, s2, 0
	s_lshl_b32 s16, s38, 7
	s_add_u32 s16, s11, s16
	s_addc_u32 s17, s2, 0
	s_ashr_i32 s11, s10, 31
	s_lshl_b32 s2, s37, 23
	s_lshl_b64 s[10:11], s[10:11], 11
	s_add_u32 s2, s21, s2
	s_addc_u32 s19, s22, 0
	s_add_u32 s2, s2, s10
	s_addc_u32 s11, s19, s11
	v_readlane_b32 s68, v255, 47
	s_add_u32 s10, s2, s18
	v_readlane_b32 s53, v255, 30
	v_readlane_b32 s56, v255, 33
	v_readlane_b32 s57, v255, 34
	v_readlane_b32 s60, v255, 37
	v_readlane_b32 s61, v255, 38
	v_readlane_b32 s62, v255, 39
	v_readlane_b32 s63, v255, 40
	v_readlane_b32 s64, v255, 41
	v_readlane_b32 s65, v255, 42
	v_readlane_b32 s66, v255, 43
	v_readlane_b32 s67, v255, 44
	v_readlane_b32 s69, v255, 48
	s_addc_u32 s11, s11, 0
	s_mov_b64 s[18:19], 0
